# baseline (speedup 1.0000x reference)
.Lmy_prio1:
.Lmy_attn_loop1:
	v_add_u32_e32 v252, s1, v158
	v_add_u32_e32 v253, 0x10800, v252
	s_waitcnt lgkmcnt(0)
	v_mfma_f32_32x32x16_bf16 v[80:95], v[196:199], v[112:115], 0
	ds_read_b128 v[128:131], v253 offset:0
	ds_read_b128 v[148:151], v253 offset:1024
	v_cvt_pk_bf16_f32 v186, v76, v77
	v_cvt_pk_bf16_f32 v187, v78, v79
	v_exp_f32_e32 v48, v48
	v_exp_f32_e32 v49, v49
	v_exp_f32_e32 v50, v50
	v_exp_f32_e32 v51, v51
	v_mfma_f32_32x32x16_bf16 v[80:95], v[108:111], v[120:123], v[80:95]
	v_exp_f32_e32 v52, v52
	v_exp_f32_e32 v53, v53
	v_exp_f32_e32 v54, v54
	v_exp_f32_e32 v55, v55
	v_mfma_f32_16x16x32_bf16 v[140:143], v[96:99], v[180:183], v[140:143]
	v_cvt_pk_bf16_f32 v172, v48, v49
	v_cvt_pk_bf16_f32 v173, v50, v51
	v_mfma_f32_32x32x16_bf16 v[0:15], v[168:171], v[180:183], v[0:15]
	v_exp_f32_e32 v56, v56
	v_exp_f32_e32 v57, v57
	v_exp_f32_e32 v58, v58
	v_exp_f32_e32 v59, v59
	v_cvt_pk_bf16_f32 v174, v52, v53
	v_cvt_pk_bf16_f32 v175, v54, v55
	v_mfma_f32_32x32x16_bf16 v[0:15], v[248:251], v[184:187], v[0:15]
	v_exp_f32_e32 v60, v60
	v_exp_f32_e32 v61, v61
	v_exp_f32_e32 v62, v62
	v_exp_f32_e32 v63, v63
	v_mfma_f32_16x16x32_bf16 v[140:143], v[96:99], v[184:187], v[140:143]
	v_cvt_pk_bf16_f32 v176, v56, v57
	v_cvt_pk_bf16_f32 v177, v58, v59
	v_mfma_f32_32x32x16_bf16 v[64:79], v[196:199], v[116:119], 0
	ds_read_b128 v[188:191], v252 offset:4096
	ds_read_b128 v[192:195], v252 offset:5120
	v_cvt_pk_bf16_f32 v178, v60, v61
	v_cvt_pk_bf16_f32 v179, v62, v63
	v_exp_f32_e32 v32, v32
	v_exp_f32_e32 v33, v33
	v_exp_f32_e32 v34, v34
	v_exp_f32_e32 v35, v35
	v_mfma_f32_32x32x16_bf16 v[64:79], v[108:111], v[124:127], v[64:79]
	v_exp_f32_e32 v36, v36
	v_exp_f32_e32 v37, v37
	v_exp_f32_e32 v38, v38
	v_exp_f32_e32 v39, v39
	v_mfma_f32_16x16x32_bf16 v[144:147], v[96:99], v[172:175], v[144:147]
	v_cvt_pk_bf16_f32 v180, v32, v33
	v_cvt_pk_bf16_f32 v181, v34, v35
	s_waitcnt lgkmcnt(2)
	v_mfma_f32_32x32x16_bf16 v[16:31], v[128:131], v[172:175], v[16:31]
	v_exp_f32_e32 v40, v40
	v_exp_f32_e32 v41, v41
	v_exp_f32_e32 v42, v42
	v_exp_f32_e32 v43, v43
	v_cvt_pk_bf16_f32 v182, v36, v37
	v_cvt_pk_bf16_f32 v183, v38, v39
	v_mfma_f32_32x32x16_bf16 v[16:31], v[148:151], v[176:179], v[16:31]
	v_exp_f32_e32 v44, v44
	v_exp_f32_e32 v45, v45
	v_exp_f32_e32 v46, v46
	v_exp_f32_e32 v47, v47
	v_mfma_f32_16x16x32_bf16 v[144:147], v[96:99], v[176:179], v[144:147]
	v_cvt_pk_bf16_f32 v184, v40, v41
	v_cvt_pk_bf16_f32 v185, v42, v43
	s_waitcnt lgkmcnt(0)
	v_mfma_f32_32x32x16_bf16 v[48:63], v[188:191], v[112:115], 0
	ds_read_b128 v[168:171], v253 offset:2048
	ds_read_b128 v[248:251], v253 offset:3072
	v_cvt_pk_bf16_f32 v186, v44, v45
	v_cvt_pk_bf16_f32 v187, v46, v47
	v_exp_f32_e32 v80, v80
	v_exp_f32_e32 v81, v81
	v_exp_f32_e32 v82, v82
	v_exp_f32_e32 v83, v83
	v_mfma_f32_32x32x16_bf16 v[48:63], v[192:195], v[120:123], v[48:63]
	v_exp_f32_e32 v84, v84
	v_exp_f32_e32 v85, v85
	v_exp_f32_e32 v86, v86
	v_exp_f32_e32 v87, v87
	v_mfma_f32_16x16x32_bf16 v[140:143], v[96:99], v[180:183], v[140:143]
	v_cvt_pk_bf16_f32 v172, v80, v81
	v_cvt_pk_bf16_f32 v173, v82, v83
	v_mfma_f32_32x32x16_bf16 v[0:15], v[128:131], v[180:183], v[0:15]
	v_exp_f32_e32 v88, v88
	v_exp_f32_e32 v89, v89
	v_exp_f32_e32 v90, v90
	v_exp_f32_e32 v91, v91
	v_cvt_pk_bf16_f32 v174, v84, v85
	v_cvt_pk_bf16_f32 v175, v86, v87
	v_mfma_f32_32x32x16_bf16 v[0:15], v[148:151], v[184:187], v[0:15]
	v_exp_f32_e32 v92, v92
	v_exp_f32_e32 v93, v93
	v_exp_f32_e32 v94, v94
	v_exp_f32_e32 v95, v95
	v_mfma_f32_16x16x32_bf16 v[140:143], v[96:99], v[184:187], v[140:143]
	v_cvt_pk_bf16_f32 v176, v88, v89
	v_cvt_pk_bf16_f32 v177, v90, v91
	v_mfma_f32_32x32x16_bf16 v[32:47], v[188:191], v[116:119], 0
	ds_read_b128 v[196:199], v252 offset:6144
	ds_read_b128 v[108:111], v252 offset:7168
	v_cvt_pk_bf16_f32 v178, v92, v93
	v_cvt_pk_bf16_f32 v179, v94, v95
	v_exp_f32_e32 v64, v64
	v_exp_f32_e32 v65, v65
	v_exp_f32_e32 v66, v66
	v_exp_f32_e32 v67, v67
	v_mfma_f32_32x32x16_bf16 v[32:47], v[192:195], v[124:127], v[32:47]
	v_exp_f32_e32 v68, v68
	v_exp_f32_e32 v69, v69
	v_exp_f32_e32 v70, v70
	v_exp_f32_e32 v71, v71
	v_mfma_f32_16x16x32_bf16 v[144:147], v[96:99], v[172:175], v[144:147]
	v_cvt_pk_bf16_f32 v180, v64, v65
	v_cvt_pk_bf16_f32 v181, v66, v67
	s_waitcnt lgkmcnt(2)
	v_mfma_f32_32x32x16_bf16 v[16:31], v[168:171], v[172:175], v[16:31]
	v_exp_f32_e32 v72, v72
	v_exp_f32_e32 v73, v73
	v_exp_f32_e32 v74, v74
	v_exp_f32_e32 v75, v75
	v_cvt_pk_bf16_f32 v182, v68, v69
	v_cvt_pk_bf16_f32 v183, v70, v71
	v_mfma_f32_32x32x16_bf16 v[16:31], v[248:251], v[176:179], v[16:31]
	v_exp_f32_e32 v76, v76
	v_exp_f32_e32 v77, v77
	v_exp_f32_e32 v78, v78
	v_exp_f32_e32 v79, v79
	v_mfma_f32_16x16x32_bf16 v[144:147], v[96:99], v[176:179], v[144:147]
	v_cvt_pk_bf16_f32 v184, v72, v73
	v_cvt_pk_bf16_f32 v185, v74, v75
	s_addk_i32 s1, 0x1000
	s_cmp_lg_u32 s1, 0x10000
	s_cbranch_scc1 .Lmy_attn_loop1
	v_cvt_pk_bf16_f32 v186, v76, v77
	v_cvt_pk_bf16_f32 v187, v78, v79
	v_mfma_f32_32x32x16_bf16 v[0:15], v[168:171], v[180:183], v[0:15]
	s_nop 0
	v_mfma_f32_16x16x32_bf16 v[140:143], v[96:99], v[180:183], v[140:143]
	v_mfma_f32_32x32x16_bf16 v[0:15], v[248:251], v[184:187], v[0:15]
	s_nop 0
	s_nop 1
	v_mfma_f32_16x16x32_bf16 v[140:143], v[96:99], v[184:187], v[140:143]
	v_lshrrev_b32_e32 v60, 2, v158
	v_and_b32_e32 v60, 60, v60
	v_and_b32_e32 v61, 0x100, v158
	v_lshrrev_b32_e32 v61, 1, v61
	v_or_b32_e32 v60, v60, v61
	s_nop 4
	ds_bpermute_b32 v61, v60, v140
	ds_bpermute_b32 v62, v60, v144
	s_waitcnt lgkmcnt(0)
	v_mul_f32_e32 v140, 0.5, v61
	v_mul_f32_e32 v144, 0.5, v62
	v_mov_b32_e32 v34, 0x3f80
	v_cmp_gt_u32_e64 s[0:1], 32, v154
	v_or_b32_e32 v36, 0x20c00, v158
	s_mov_b32 s2, 0x3f803f80
	v_cndmask_b32_e64 v96, 0, v34, s[0:1]
	v_or_b32_e32 v34, 0x20800, v158
	ds_read_b128 v[108:111], v34
	ds_read_b128 v[128:131], v36
	v_exp_f32_e32 v34, v48
	v_exp_f32_e32 v35, v49
	s_mov_b32 s3, s2
	v_mov_b64_e32 v[52:53], s[2:3]
	v_exp_f32_e32 v32, v32
	v_exp_f32_e32 v33, v33
	v_mov_b32_e32 v97, 0
	v_cndmask_b32_e64 v34, 0, v34, s[0:1]
	v_cndmask_b32_e64 v35, 0, v35, s[0:1]
	v_cvt_pk_bf16_f32 v34, v34, v35
	v_mov_b32_e32 v35, v97
	v_mov_b32_e32 v36, v97
	v_mov_b32_e32 v37, v97
	s_mov_b32 s8, 0
	v_cndmask_b32_e64 v32, 0, v32, s[0:1]
	v_cndmask_b32_e64 v33, 0, v33, s[0:1]
	s_waitcnt lgkmcnt(1)
	v_mfma_f32_32x32x16_bf16 v[16:31], v[108:111], v[34:37], v[16:31]
	s_mov_b32 s9, s8
	v_cvt_pk_bf16_f32 v46, v32, v33
	v_mov_b64_e32 v[50:51], s[8:9]
	v_mov_b32_e32 v32, v46
	v_mov_b32_e32 v33, v97
	v_mov_b32_e32 v47, v97
	v_mov_b32_e32 v48, v97
	v_mfma_f32_4x4x4_16b_bf16 v[34:37], v[52:53], v[34:35], v[144:147]
	v_mov_b32_e32 v49, v97
	s_mov_b32 s10, s8
	v_mfma_f32_4x4x4_16b_bf16 v[38:41], v[52:53], v[50:51], v[34:37]
	s_mov_b32 s11, s8
	v_mfma_f32_4x4x4_16b_bf16 v[32:35], v[52:53], v[32:33], v[140:143]
	v_mov_b64_e32 v[44:45], s[10:11]
	v_mfma_f32_32x32x16_bf16 v[0:15], v[108:111], v[46:49], v[0:15]
	v_mov_b64_e32 v[42:43], s[8:9]
	s_mov_b32 s7, 0x7149f2ca
	s_mov_b32 s4, 0xda24260
	v_mov_b32_e32 v98, v97
	v_mov_b32_e32 v99, v97
	v_mfma_f32_4x4x4_16b_bf16 v[32:35], v[52:53], v[50:51], v[32:35]
	s_waitcnt lgkmcnt(0)
	v_mfma_f32_32x32x16_bf16 v[16:31], v[128:131], v[42:45], v[16:31]
	s_nop 2
	v_mbcnt_lo_u32_b32 v33, -1, 0
	v_mbcnt_hi_u32_b32 v33, -1, v33
	v_and_b32_e32 v35, 64, v33
	v_xor_b32_e32 v34, 32, v33
	v_add_u32_e32 v35, 64, v35
	v_cmp_lt_i32_e32 vcc, v34, v35
	v_mfma_f32_32x32x16_bf16 v[0:15], v[128:131], v[42:45], v[0:15]
	s_nop 0
	v_cndmask_b32_e32 v33, v33, v34, vcc
	v_lshlrev_b32_e32 v165, 2, v33
	ds_bpermute_b32 v35, v165, v38
	ds_bpermute_b32 v34, v165, v32
	v_mov_b32_e32 v33, v38
	s_waitcnt lgkmcnt(0)
	v_pk_add_f32 v[34:35], v[32:33], v[34:35]
	s_nop 0
	v_cmp_ngt_f32_e32 vcc, s7, v35
	v_cmp_nlt_f32_e64 s[2:3], s4, v34
	v_cmp_nlt_f32_e64 s[4:5], s4, v35
	s_or_b64 s[4:5], s[4:5], vcc
	v_cmp_ngt_f32_e32 vcc, s7, v34
	s_or_b64 s[2:3], s[2:3], vcc
	s_or_b64 vcc, s[4:5], s[2:3]
	s_cbranch_vccnz .LBB6_40

.Lmy_prio2:
.Lmy_attn_loop2:
	v_add_u32_e32 v248, s27, v158
	v_add_u32_e32 v249, 0x10800, v248
	s_waitcnt lgkmcnt(0)
	v_mfma_f32_32x32x16_bf16 v[80:95], v[224:227], v[100:103], 0
	ds_read_b128 v[232:235], v249 offset:0
	ds_read_b128 v[236:239], v249 offset:1024
	v_cvt_pk_bf16_f32 v186, v76, v77
	v_cvt_pk_bf16_f32 v187, v78, v79
	v_exp_f32_e32 v48, v48
	v_exp_f32_e32 v49, v49
	v_exp_f32_e32 v50, v50
	v_exp_f32_e32 v51, v51
	v_mfma_f32_32x32x16_bf16 v[80:95], v[228:231], v[108:111], v[80:95]
	v_exp_f32_e32 v52, v52
	v_exp_f32_e32 v53, v53
	v_exp_f32_e32 v54, v54
	v_exp_f32_e32 v55, v55
	v_mfma_f32_16x16x32_bf16 v[136:139], v[116:119], v[180:183], v[136:139]
	v_cvt_pk_bf16_f32 v172, v48, v49
	v_cvt_pk_bf16_f32 v173, v50, v51
	v_mfma_f32_32x32x16_bf16 v[0:15], v[240:243], v[180:183], v[0:15]
	v_exp_f32_e32 v56, v56
	v_exp_f32_e32 v57, v57
	v_exp_f32_e32 v58, v58
	v_exp_f32_e32 v59, v59
	v_cvt_pk_bf16_f32 v174, v52, v53
	v_cvt_pk_bf16_f32 v175, v54, v55
	v_mfma_f32_32x32x16_bf16 v[0:15], v[244:247], v[184:187], v[0:15]
	v_exp_f32_e32 v60, v60
	v_exp_f32_e32 v61, v61
	v_exp_f32_e32 v62, v62
	v_exp_f32_e32 v63, v63
	v_mfma_f32_16x16x32_bf16 v[136:139], v[116:119], v[184:187], v[136:139]
	v_cvt_pk_bf16_f32 v176, v56, v57
	v_cvt_pk_bf16_f32 v177, v58, v59
	v_mfma_f32_32x32x16_bf16 v[64:79], v[224:227], v[104:107], 0
	ds_read_b128 v[216:219], v248 offset:4096
	ds_read_b128 v[220:223], v248 offset:5120
	v_cvt_pk_bf16_f32 v178, v60, v61
	v_cvt_pk_bf16_f32 v179, v62, v63
	v_exp_f32_e32 v32, v32
	v_exp_f32_e32 v33, v33
	v_exp_f32_e32 v34, v34
	v_exp_f32_e32 v35, v35
	v_mfma_f32_32x32x16_bf16 v[64:79], v[228:231], v[112:115], v[64:79]
	v_exp_f32_e32 v36, v36
	v_exp_f32_e32 v37, v37
	v_exp_f32_e32 v38, v38
	v_exp_f32_e32 v39, v39
	v_mfma_f32_16x16x32_bf16 v[140:143], v[116:119], v[172:175], v[140:143]
	v_cvt_pk_bf16_f32 v180, v32, v33
	v_cvt_pk_bf16_f32 v181, v34, v35
	s_waitcnt lgkmcnt(2)
	v_mfma_f32_32x32x16_bf16 v[16:31], v[232:235], v[172:175], v[16:31]
	v_exp_f32_e32 v40, v40
	v_exp_f32_e32 v41, v41
	v_exp_f32_e32 v42, v42
	v_exp_f32_e32 v43, v43
	v_cvt_pk_bf16_f32 v182, v36, v37
	v_cvt_pk_bf16_f32 v183, v38, v39
	v_mfma_f32_32x32x16_bf16 v[16:31], v[236:239], v[176:179], v[16:31]
	v_exp_f32_e32 v44, v44
	v_exp_f32_e32 v45, v45
	v_exp_f32_e32 v46, v46
	v_exp_f32_e32 v47, v47
	v_mfma_f32_16x16x32_bf16 v[140:143], v[116:119], v[176:179], v[140:143]
	v_cvt_pk_bf16_f32 v184, v40, v41
	v_cvt_pk_bf16_f32 v185, v42, v43
	s_waitcnt lgkmcnt(0)
	v_mfma_f32_32x32x16_bf16 v[48:63], v[216:219], v[100:103], 0
	ds_read_b128 v[240:243], v249 offset:2048
	ds_read_b128 v[244:247], v249 offset:3072
	v_cvt_pk_bf16_f32 v186, v44, v45
	v_cvt_pk_bf16_f32 v187, v46, v47
	v_exp_f32_e32 v80, v80
	v_exp_f32_e32 v81, v81
	v_exp_f32_e32 v82, v82
	v_exp_f32_e32 v83, v83
	v_mfma_f32_32x32x16_bf16 v[48:63], v[220:223], v[108:111], v[48:63]
	v_exp_f32_e32 v84, v84
	v_exp_f32_e32 v85, v85
	v_exp_f32_e32 v86, v86
	v_exp_f32_e32 v87, v87
	v_mfma_f32_16x16x32_bf16 v[136:139], v[116:119], v[180:183], v[136:139]
	v_cvt_pk_bf16_f32 v172, v80, v81
	v_cvt_pk_bf16_f32 v173, v82, v83
	v_mfma_f32_32x32x16_bf16 v[0:15], v[232:235], v[180:183], v[0:15]
	v_exp_f32_e32 v88, v88
	v_exp_f32_e32 v89, v89
	v_exp_f32_e32 v90, v90
	v_exp_f32_e32 v91, v91
	v_cvt_pk_bf16_f32 v174, v84, v85
	v_cvt_pk_bf16_f32 v175, v86, v87
	v_mfma_f32_32x32x16_bf16 v[0:15], v[236:239], v[184:187], v[0:15]
	v_exp_f32_e32 v92, v92
	v_exp_f32_e32 v93, v93
	v_exp_f32_e32 v94, v94
	v_exp_f32_e32 v95, v95
	v_mfma_f32_16x16x32_bf16 v[136:139], v[116:119], v[184:187], v[136:139]
	v_cvt_pk_bf16_f32 v176, v88, v89
	v_cvt_pk_bf16_f32 v177, v90, v91
	v_mfma_f32_32x32x16_bf16 v[32:47], v[216:219], v[104:107], 0
	ds_read_b128 v[224:227], v248 offset:6144
	ds_read_b128 v[228:231], v248 offset:7168
	v_cvt_pk_bf16_f32 v178, v92, v93
	v_cvt_pk_bf16_f32 v179, v94, v95
	v_exp_f32_e32 v64, v64
	v_exp_f32_e32 v65, v65
	v_exp_f32_e32 v66, v66
	v_exp_f32_e32 v67, v67
	v_mfma_f32_32x32x16_bf16 v[32:47], v[220:223], v[112:115], v[32:47]
	v_exp_f32_e32 v68, v68
	v_exp_f32_e32 v69, v69
	v_exp_f32_e32 v70, v70
	v_exp_f32_e32 v71, v71
	v_mfma_f32_16x16x32_bf16 v[140:143], v[116:119], v[172:175], v[140:143]
	v_cvt_pk_bf16_f32 v180, v64, v65
	v_cvt_pk_bf16_f32 v181, v66, v67
	s_waitcnt lgkmcnt(2)
	v_mfma_f32_32x32x16_bf16 v[16:31], v[240:243], v[172:175], v[16:31]
	v_exp_f32_e32 v72, v72
	v_exp_f32_e32 v73, v73
	v_exp_f32_e32 v74, v74
	v_exp_f32_e32 v75, v75
	v_cvt_pk_bf16_f32 v182, v68, v69
	v_cvt_pk_bf16_f32 v183, v70, v71
	v_mfma_f32_32x32x16_bf16 v[16:31], v[244:247], v[176:179], v[16:31]
	v_exp_f32_e32 v76, v76
	v_exp_f32_e32 v77, v77
	v_exp_f32_e32 v78, v78
	v_exp_f32_e32 v79, v79
	v_mfma_f32_16x16x32_bf16 v[140:143], v[116:119], v[176:179], v[140:143]
	v_cvt_pk_bf16_f32 v184, v72, v73
	v_cvt_pk_bf16_f32 v185, v74, v75
	s_addk_i32 s27, 0x1000
	s_cmp_lg_u32 s27, 0x10000
	s_cbranch_scc1 .Lmy_attn_loop2
	v_cvt_pk_bf16_f32 v186, v76, v77
	v_cvt_pk_bf16_f32 v187, v78, v79
	v_mfma_f32_32x32x16_bf16 v[0:15], v[240:243], v[180:183], v[0:15]
	s_nop 0
	v_mfma_f32_16x16x32_bf16 v[136:139], v[116:119], v[180:183], v[136:139]
	v_mfma_f32_32x32x16_bf16 v[0:15], v[244:247], v[184:187], v[0:15]
	s_nop 0
	s_nop 1
	v_mfma_f32_16x16x32_bf16 v[136:139], v[116:119], v[184:187], v[136:139]
	s_setprio 0
	v_lshrrev_b32_e32 v60, 2, v158
	v_and_b32_e32 v60, 60, v60
	v_and_b32_e32 v61, 0x100, v158
	v_lshrrev_b32_e32 v61, 1, v61
	v_or_b32_e32 v60, v60, v61
	s_nop 4
	ds_bpermute_b32 v61, v60, v136
	ds_bpermute_b32 v62, v60, v140
	s_waitcnt lgkmcnt(0)
	v_mul_f32_e32 v136, 0.5, v61
	v_mul_f32_e32 v140, 0.5, v62
	v_or_b32_e32 v34, 0x20800, v158
	ds_read_b128 v[116:119], v34
	v_or_b32_e32 v36, 0x20c00, v158
	s_mov_b32 s4, 0x3f803f80
	v_exp_f32_e32 v35, v49
	ds_read_b128 v[120:123], v36
	v_exp_f32_e32 v34, v48
	s_mov_b32 s5, s4
	v_mov_b64_e32 v[46:47], s[4:5]
	v_exp_f32_e32 v38, v32
	v_exp_f32_e32 v39, v33
	v_cndmask_b32_e64 v34, 0, v34, s[0:1]
	v_cndmask_b32_e64 v35, 0, v35, s[0:1]
	v_mov_b32_e32 v125, 0
	v_cvt_pk_bf16_f32 v124, v34, v35
	v_mov_b32_e32 v126, v125
	v_mov_b32_e32 v127, v125
	v_cndmask_b32_e64 v38, 0, v38, s[0:1]
	v_cndmask_b32_e64 v39, 0, v39, s[0:1]
	s_waitcnt lgkmcnt(1)
	v_mfma_f32_32x32x16_bf16 v[16:31], v[116:119], v[124:127], v[16:31]
	s_mov_b32 s8, 0
	s_mov_b32 s9, s8
	v_mov_b64_e32 v[36:37], s[8:9]
	s_mov_b32 s10, s8
	s_mov_b32 s11, s8
	v_mov_b64_e32 v[44:45], s[10:11]
	v_mov_b64_e32 v[42:43], s[8:9]
	v_mfma_f32_4x4x4_16b_bf16 v[32:35], v[46:47], v[124:125], v[140:143]
	v_cvt_pk_bf16_f32 v124, v38, v39
	s_waitcnt lgkmcnt(0)
	v_mfma_f32_32x32x16_bf16 v[16:31], v[120:123], v[42:45], v[16:31]
	s_mov_b32 s9, 0x7149f2ca
	s_mov_b32 s6, 0xda24260
	v_mfma_f32_32x32x16_bf16 v[0:15], v[116:119], v[124:127], v[0:15]
	v_mfma_f32_4x4x4_16b_bf16 v[38:41], v[46:47], v[36:37], v[32:35]
	v_mfma_f32_4x4x4_16b_bf16 v[32:35], v[46:47], v[124:125], v[136:139]
	v_mfma_f32_32x32x16_bf16 v[0:15], v[120:123], v[42:45], v[0:15]
	s_nop 0
	v_mfma_f32_4x4x4_16b_bf16 v[32:35], v[46:47], v[36:37], v[32:35]
	s_nop 4
	ds_bpermute_b32 v35, v165, v38
	ds_bpermute_b32 v34, v165, v32
	v_mov_b32_e32 v33, v38
	s_waitcnt lgkmcnt(0)
	v_pk_add_f32 v[34:35], v[32:33], v[34:35]
	s_nop 0
	v_cmp_ngt_f32_e32 vcc, s9, v35
	v_cmp_nlt_f32_e64 s[4:5], s6, v34
	v_cmp_nlt_f32_e64 s[6:7], s6, v35
	s_or_b64 s[6:7], s[6:7], vcc
	v_cmp_ngt_f32_e32 vcc, s9, v34
	s_or_b64 s[4:5], s[4:5], vcc
	s_or_b64 vcc, s[6:7], s[4:5]
	s_cbranch_vccnz .LBB6_64
